# also removed the dead abs-max reduction and store of the unused int8 activation scale (SX) in the combine phase and the x conversion loop
# speedup vs baseline: 1.0095x; 1.0034x over previous
; __device__ __forceinline__ unsigned pk2(float lo, float hi) { unsigned r; asm("v_cvt_pk_bf16_f32 %0, %1, %2" : "=v"(r) : "v"(lo), "v"(hi)); return r; }
; __device__ __forceinline__ void phase_convert(CArgs a, LAS unsigned char* lds, int wv) {
;     ...
;       for (int tok = gw; tok < NTOK; tok += NGW) { f32x4 v[2][2]; float am = 0.f;
; #pragma unroll
;           for (int j = 0; j < 2; ++j) { v[j][0] = *(const f32x4*)(x + (size_t)tok * DM + lane * 8 + 512 * j); v[j][1] = *(const f32x4*)(x + (size_t)tok * DM + lane * 8 + 512 * j + 4);
;               const f32x4 a0 = __builtin_elementwise_abs(v[j][0]), a1 = __builtin_elementwise_abs(v[j][1]); am = fmaxf(am, fmaxf(fmaxf(fmaxf(a0.x, a0.y), fmaxf(a0.z, a0.w)), fmaxf(fmaxf(a1.x, a1.y), fmaxf(a1.z, a1.w)))); }
;           am = fmaxf(wave_max(am, lane), 1e-20f); const float inv = 127.f / am; if (lane == 0) SX[tok] = am * (1.f / 127.f);
; #pragma unroll
;           for (int j = 0; j < 2; ++j) { const int c0 = lane * 8 + 512 * j;
;               u32x4 w; w.x = pk2(v[j][0].x, v[j][0].y); w.y = pk2(v[j][0].z, v[j][0].w); w.z = pk2(v[j][1].x, v[j][1].y); w.w = pk2(v[j][1].z, v[j][1].w); *(u32x4*)(XB + (size_t)tok * DM + c0) = w;
;               if (FP6_IN) { const unsigned pk[4] = {pk2(v[j][0].x * QS_XQ, v[j][0].y * QS_XQ), pk2(v[j][0].z * QS_XQ, v[j][0].w * QS_XQ), pk2(v[j][1].x * QS_XQ, v[j][1].y * QS_XQ), pk2(v[j][1].z * QS_XQ, v[j][1].w * QS_XQ)};
;                   store_fp6_quad(XQ + (size_t)tok * DM, (lane >> 2) + 16 * j, pk, lane, j); }
.LBB0_94:
	v_cvt_pk_bf16_f32 v8, v4, v5
	v_lshl_add_u64 v[34:35], s[12:13], 0, v[24:25]
	v_mul_f32_e32 v4, 0x3fe00000, v4
	v_mul_f32_e32 v5, 0x3fe00000, v5
	s_waitcnt lgkmcnt(0)
	v_cvt_pk_bf16_f32 v9, v6, v7
	v_cvt_pk_bf16_f32 v10, v0, v1
	v_add_co_u32_e32 v12, vcc, 0x38000000, v34
	v_cvt_pk_bf16_f32 v5, v4, v5
	v_mul_f32_e32 v4, 0x3fe00000, v6
	v_mul_f32_e32 v6, 0x3fe00000, v7
	v_mul_f32_e32 v0, 0x3fe00000, v0
	v_mul_f32_e32 v1, 0x3fe00000, v1
	v_cvt_pk_bf16_f32 v11, v2, v3
	v_addc_co_u32_e32 v13, vcc, 0, v35, vcc
	v_cvt_pk_bf16_f32 v6, v4, v6
	v_cvt_pk_bf16_f32 v7, v0, v1
	v_mul_f32_e32 v0, 0x3fe00000, v2
	v_mul_f32_e32 v1, 0x3fe00000, v3
	v_cvt_pk_bf16_f32 v15, v0, v1
	global_store_dwordx4 v[12:13], v[8:11], off
	v_mov_b32_dpp v0, v5 quad_perm:[0,0,0,0] row_mask:0xf bank_mask:0xf bound_ctrl:1
	v_mov_b32_dpp v4, v5 quad_perm:[1,1,1,1] row_mask:0xf bank_mask:0xf bound_ctrl:1
	v_mov_b32_dpp v8, v5 quad_perm:[2,2,2,2] row_mask:0xf bank_mask:0xf bound_ctrl:1
	v_mov_b32_dpp v12, v5 quad_perm:[3,3,3,3] row_mask:0xf bank_mask:0xf bound_ctrl:1
	v_mov_b32_dpp v1, v6 quad_perm:[0,0,0,0] row_mask:0xf bank_mask:0xf bound_ctrl:1
	v_mov_b32_dpp v5, v6 quad_perm:[1,1,1,1] row_mask:0xf bank_mask:0xf bound_ctrl:1
	v_mov_b32_dpp v9, v6 quad_perm:[2,2,2,2] row_mask:0xf bank_mask:0xf bound_ctrl:1
	v_mov_b32_dpp v13, v6 quad_perm:[3,3,3,3] row_mask:0xf bank_mask:0xf bound_ctrl:1
	v_mov_b32_dpp v2, v7 quad_perm:[0,0,0,0] row_mask:0xf bank_mask:0xf bound_ctrl:1
	v_mov_b32_dpp v6, v7 quad_perm:[1,1,1,1] row_mask:0xf bank_mask:0xf bound_ctrl:1
	v_mov_b32_dpp v10, v7 quad_perm:[2,2,2,2] row_mask:0xf bank_mask:0xf bound_ctrl:1
	v_mov_b32_dpp v14, v7 quad_perm:[3,3,3,3] row_mask:0xf bank_mask:0xf bound_ctrl:1
	v_mov_b32_dpp v3, v15 quad_perm:[0,0,0,0] row_mask:0xf bank_mask:0xf bound_ctrl:1
	v_mov_b32_dpp v7, v15 quad_perm:[1,1,1,1] row_mask:0xf bank_mask:0xf bound_ctrl:1
	v_mov_b32_dpp v11, v15 quad_perm:[2,2,2,2] row_mask:0xf bank_mask:0xf bound_ctrl:1
	v_mov_b32_dpp v15, v15 quad_perm:[3,3,3,3] row_mask:0xf bank_mask:0xf bound_ctrl:1
	v_lshl_add_u64 v[32:33], s[12:13], 0, v[30:31]
	s_and_saveexec_b64 s[24:25], s[6:7]
	s_cbranch_execz .LBB0_96
	v_cvt_scalef32_pk32_fp6_bf16 v[42:47], v[0:15], 1.0
	v_mov_b32_e32 v0, v46
	v_mov_b32_e32 v1, v47
	v_mov_b32_e32 v2, v46
	v_mov_b32_e32 v3, v47
	global_store_dwordx4 v[32:33], v[42:45], off offset:-512
	global_store_dwordx4 v[32:33], v[0:3], off offset:-448

; __device__ __forceinline__ unsigned pk2(float lo, float hi) { unsigned r; asm("v_cvt_pk_bf16_f32 %0, %1, %2" : "=v"(r) : "v"(lo), "v"(hi)); return r; }
; __device__ __forceinline__ void phase_combine(CArgs a, LAS unsigned char* lds, int L, int wv, int xw  ) {
;     ...
;             float am = 0.f;
; #pragma unroll
;             for (int j = 0; j < 2; ++j) { const int c0 = lane * 8 + 512 * j;
;                 v[h][j][0] = v[h][j][0] * rstd * *(const f32x4*)(lng + c0) + *(const f32x4*)(lnb + c0); v[h][j][1] = v[h][j][1] * rstd * *(const f32x4*)(lng + c0 + 4) + *(const f32x4*)(lnb + c0 + 4);
;                 const f32x4 a0 = __builtin_elementwise_abs(v[h][j][0]), a1 = __builtin_elementwise_abs(v[h][j][1]); am = fmaxf(am, fmaxf(fmaxf(fmaxf(a0.x, a0.y), fmaxf(a0.z, a0.w)), fmaxf(fmaxf(a1.x, a1.y), fmaxf(a1.z, a1.w)))); }
;             if (last) {
; #pragma unroll
;                 for (int j = 0; j < 2; ++j) { const int c0 = lane * 8 + 512 * j; *(f32x4*)(OUT + (size_t)tok * DM + c0) = v[h][j][0]; *(f32x4*)(OUT + (size_t)tok * DM + c0 + 4) = v[h][j][1]; } }
;             else {
;                 am = fmaxf(wave_max(am, lane), 1e-20f); const float inv = 127.f / am; if (lane == 0) SX[tok] = am * (1.f / 127.f);
; #pragma unroll
;                 for (int j = 0; j < 2; ++j) { const int c0 = lane * 8 + 512 * j; const f32x4 x0 = v[h][j][0], x1 = v[h][j][1];
;                     u32x4 w; w.x = pk2(x0.x, x0.y); w.y = pk2(x0.z, x0.w); w.z = pk2(x1.x, x1.y); w.w = pk2(x1.z, x1.w); *(u32x4*)(XB + (size_t)tok * DM + c0) = w;
;                     if (FP6_IN) { const unsigned pk[4] = {pk2(x0.x * QS_XQ, x0.y * QS_XQ), pk2(x0.z * QS_XQ, x0.w * QS_XQ), pk2(x1.x * QS_XQ, x1.y * QS_XQ), pk2(x1.z * QS_XQ, x1.w * QS_XQ)};
;                         store_fp6_quad(XQ + (size_t)tok * DM, (lane >> 2) + 16 * j, pk, lane, j); }
.LBB0_922:
	v_cvt_pk_bf16_f32 v0, v84, v85
	s_waitcnt lgkmcnt(0)
	v_cvt_pk_bf16_f32 v1, v86, v87
	v_lshl_add_u64 v[176:177], v[114:115], 0, s[30:31]
	v_cvt_pk_bf16_f32 v2, v88, v89
	v_cvt_pk_bf16_f32 v3, v90, v91
	global_store_dwordx4 v[176:177], v[0:3], off
	s_lshl_b64 s[12:13], s[26:27], 10
	v_mul_f32_e32 v4, 0x3fe00000, v91
	v_mul_f32_e32 v0, 0x3fe00000, v84
	v_mul_f32_e32 v1, 0x3fe00000, v85
	v_cvt_pk_bf16_f32 v1, v0, v1
	v_mul_f32_e32 v0, 0x3fe00000, v86
	v_mul_f32_e32 v2, 0x3fe00000, v87
	v_cvt_pk_bf16_f32 v2, v0, v2
	v_mul_f32_e32 v0, 0x3fe00000, v88
	v_mul_f32_e32 v3, 0x3fe00000, v89
	v_cvt_pk_bf16_f32 v3, v0, v3
	v_mul_f32_e32 v0, 0x3fe00000, v90
	v_cvt_pk_bf16_f32 v15, v0, v4
	v_lshl_add_u64 v[174:175], v[102:103], 0, s[12:13]
	v_mov_b32_dpp v4, v1 quad_perm:[1,1,1,1] row_mask:0xf bank_mask:0xf bound_ctrl:1
	v_mov_b32_dpp v0, v1 quad_perm:[0,0,0,0] row_mask:0xf bank_mask:0xf bound_ctrl:1
	v_mov_b32_dpp v8, v1 quad_perm:[2,2,2,2] row_mask:0xf bank_mask:0xf bound_ctrl:1
	v_mov_b32_dpp v12, v1 quad_perm:[3,3,3,3] row_mask:0xf bank_mask:0xf bound_ctrl:1
	v_mov_b32_dpp v1, v2 quad_perm:[0,0,0,0] row_mask:0xf bank_mask:0xf bound_ctrl:1
	v_mov_b32_dpp v5, v2 quad_perm:[1,1,1,1] row_mask:0xf bank_mask:0xf bound_ctrl:1
	v_mov_b32_dpp v9, v2 quad_perm:[2,2,2,2] row_mask:0xf bank_mask:0xf bound_ctrl:1
	v_mov_b32_dpp v13, v2 quad_perm:[3,3,3,3] row_mask:0xf bank_mask:0xf bound_ctrl:1
	v_mov_b32_dpp v2, v3 quad_perm:[0,0,0,0] row_mask:0xf bank_mask:0xf bound_ctrl:1
	v_mov_b32_dpp v6, v3 quad_perm:[1,1,1,1] row_mask:0xf bank_mask:0xf bound_ctrl:1
	v_mov_b32_dpp v10, v3 quad_perm:[2,2,2,2] row_mask:0xf bank_mask:0xf bound_ctrl:1
	v_mov_b32_dpp v14, v3 quad_perm:[3,3,3,3] row_mask:0xf bank_mask:0xf bound_ctrl:1
	v_mov_b32_dpp v3, v15 quad_perm:[0,0,0,0] row_mask:0xf bank_mask:0xf bound_ctrl:1
	v_mov_b32_dpp v7, v15 quad_perm:[1,1,1,1] row_mask:0xf bank_mask:0xf bound_ctrl:1
	v_mov_b32_dpp v11, v15 quad_perm:[2,2,2,2] row_mask:0xf bank_mask:0xf bound_ctrl:1
	v_mov_b32_dpp v15, v15 quad_perm:[3,3,3,3] row_mask:0xf bank_mask:0xf bound_ctrl:1
	s_and_saveexec_b64 s[12:13], s[8:9]
	s_cbranch_execz .LBB0_924
	v_lshl_add_u64 v[178:179], v[174:175], 0, v[100:101]
	v_cvt_scalef32_pk32_fp6_bf16 v[198:203], v[0:15], 1.0
	v_mov_b32_e32 v0, v202
	v_mov_b32_e32 v1, v203
	v_mov_b32_e32 v2, v202
	v_mov_b32_e32 v3, v203
	global_store_dwordx4 v[178:179], v[198:201], off
	global_store_dwordx4 v[178:179], v[0:3], off offset:64

; __device__ __forceinline__ unsigned pk2(float lo, float hi) { unsigned r; asm("v_cvt_pk_bf16_f32 %0, %1, %2" : "=v"(r) : "v"(lo), "v"(hi)); return r; }
; __device__ __forceinline__ void phase_combine(CArgs a, LAS unsigned char* lds, int L, int wv, int xw  ) {
;     ...
;             float am = 0.f;
; #pragma unroll
;             for (int j = 0; j < 2; ++j) { const int c0 = lane * 8 + 512 * j;
;                 v[h][j][0] = v[h][j][0] * rstd * *(const f32x4*)(lng + c0) + *(const f32x4*)(lnb + c0); v[h][j][1] = v[h][j][1] * rstd * *(const f32x4*)(lng + c0 + 4) + *(const f32x4*)(lnb + c0 + 4);
;                 const f32x4 a0 = __builtin_elementwise_abs(v[h][j][0]), a1 = __builtin_elementwise_abs(v[h][j][1]); am = fmaxf(am, fmaxf(fmaxf(fmaxf(a0.x, a0.y), fmaxf(a0.z, a0.w)), fmaxf(fmaxf(a1.x, a1.y), fmaxf(a1.z, a1.w)))); }
;             if (last) {
; #pragma unroll
;                 for (int j = 0; j < 2; ++j) { const int c0 = lane * 8 + 512 * j; *(f32x4*)(OUT + (size_t)tok * DM + c0) = v[h][j][0]; *(f32x4*)(OUT + (size_t)tok * DM + c0 + 4) = v[h][j][1]; } }
;             else {
;                 am = fmaxf(wave_max(am, lane), 1e-20f); const float inv = 127.f / am; if (lane == 0) SX[tok] = am * (1.f / 127.f);
; #pragma unroll
;                 for (int j = 0; j < 2; ++j) { const int c0 = lane * 8 + 512 * j; const f32x4 x0 = v[h][j][0], x1 = v[h][j][1];
;                     u32x4 w; w.x = pk2(x0.x, x0.y); w.y = pk2(x0.z, x0.w); w.z = pk2(x1.x, x1.y); w.w = pk2(x1.z, x1.w); *(u32x4*)(XB + (size_t)tok * DM + c0) = w;
;                     if (FP6_IN) { const unsigned pk[4] = {pk2(x0.x * QS_XQ, x0.y * QS_XQ), pk2(x0.z * QS_XQ, x0.w * QS_XQ), pk2(x1.x * QS_XQ, x1.y * QS_XQ), pk2(x1.z * QS_XQ, x1.w * QS_XQ)};
;                         store_fp6_quad(XQ + (size_t)tok * DM, (lane >> 2) + 16 * j, pk, lane, j); }
.LBB0_932:
	v_cvt_pk_bf16_f32 v0, v72, v73
	s_waitcnt lgkmcnt(0)
	v_cvt_pk_bf16_f32 v1, v74, v75
	v_lshl_add_u64 v[90:91], v[114:115], 0, s[24:25]
	v_cvt_pk_bf16_f32 v2, v76, v77
	v_cvt_pk_bf16_f32 v3, v78, v79
	global_store_dwordx4 v[90:91], v[0:3], off
	s_lshl_b64 s[26:27], s[14:15], 10
	v_mul_f32_e32 v4, 0x3fe00000, v79
	v_mul_f32_e32 v0, 0x3fe00000, v72
	v_mul_f32_e32 v1, 0x3fe00000, v73
	v_cvt_pk_bf16_f32 v1, v0, v1
	v_mul_f32_e32 v0, 0x3fe00000, v74
	v_mul_f32_e32 v2, 0x3fe00000, v75
	v_cvt_pk_bf16_f32 v2, v0, v2
	v_mul_f32_e32 v0, 0x3fe00000, v76
	v_mul_f32_e32 v3, 0x3fe00000, v77
	v_cvt_pk_bf16_f32 v3, v0, v3
	v_mul_f32_e32 v0, 0x3fe00000, v78
	v_cvt_pk_bf16_f32 v15, v0, v4
	v_lshl_add_u64 v[88:89], v[102:103], 0, s[26:27]
	v_mov_b32_dpp v4, v1 quad_perm:[1,1,1,1] row_mask:0xf bank_mask:0xf bound_ctrl:1
	v_mov_b32_dpp v0, v1 quad_perm:[0,0,0,0] row_mask:0xf bank_mask:0xf bound_ctrl:1
	v_mov_b32_dpp v8, v1 quad_perm:[2,2,2,2] row_mask:0xf bank_mask:0xf bound_ctrl:1
	v_mov_b32_dpp v12, v1 quad_perm:[3,3,3,3] row_mask:0xf bank_mask:0xf bound_ctrl:1
	v_mov_b32_dpp v1, v2 quad_perm:[0,0,0,0] row_mask:0xf bank_mask:0xf bound_ctrl:1
	v_mov_b32_dpp v5, v2 quad_perm:[1,1,1,1] row_mask:0xf bank_mask:0xf bound_ctrl:1
	v_mov_b32_dpp v9, v2 quad_perm:[2,2,2,2] row_mask:0xf bank_mask:0xf bound_ctrl:1
	v_mov_b32_dpp v13, v2 quad_perm:[3,3,3,3] row_mask:0xf bank_mask:0xf bound_ctrl:1
	v_mov_b32_dpp v2, v3 quad_perm:[0,0,0,0] row_mask:0xf bank_mask:0xf bound_ctrl:1
	v_mov_b32_dpp v6, v3 quad_perm:[1,1,1,1] row_mask:0xf bank_mask:0xf bound_ctrl:1
	v_mov_b32_dpp v10, v3 quad_perm:[2,2,2,2] row_mask:0xf bank_mask:0xf bound_ctrl:1
	v_mov_b32_dpp v14, v3 quad_perm:[3,3,3,3] row_mask:0xf bank_mask:0xf bound_ctrl:1
	v_mov_b32_dpp v3, v15 quad_perm:[0,0,0,0] row_mask:0xf bank_mask:0xf bound_ctrl:1
	v_mov_b32_dpp v7, v15 quad_perm:[1,1,1,1] row_mask:0xf bank_mask:0xf bound_ctrl:1
	v_mov_b32_dpp v11, v15 quad_perm:[2,2,2,2] row_mask:0xf bank_mask:0xf bound_ctrl:1
	v_mov_b32_dpp v15, v15 quad_perm:[3,3,3,3] row_mask:0xf bank_mask:0xf bound_ctrl:1
	s_and_saveexec_b64 s[24:25], s[8:9]
	s_cbranch_execz .LBB0_934
	v_lshl_add_u64 v[98:99], v[88:89], 0, v[100:101]
	v_cvt_scalef32_pk32_fp6_bf16 v[92:97], v[0:15], 1.0
	v_mov_b32_e32 v0, v96
	v_mov_b32_e32 v1, v97
	v_mov_b32_e32 v2, v96
	v_mov_b32_e32 v3, v97
	global_store_dwordx4 v[98:99], v[92:95], off
	global_store_dwordx4 v[98:99], v[0:3], off offset:64

; __device__ __forceinline__ unsigned pk2(float lo, float hi) { unsigned r; asm("v_cvt_pk_bf16_f32 %0, %1, %2" : "=v"(r) : "v"(lo), "v"(hi)); return r; }
; __device__ __forceinline__ void phase_combine(CArgs a, LAS unsigned char* lds, int L, int wv, int xw  ) {
;     ...
;             float am = 0.f;
; #pragma unroll
;             for (int j = 0; j < 2; ++j) { const int c0 = lane * 8 + 512 * j;
;                 v[h][j][0] = v[h][j][0] * rstd * *(const f32x4*)(lng + c0) + *(const f32x4*)(lnb + c0); v[h][j][1] = v[h][j][1] * rstd * *(const f32x4*)(lng + c0 + 4) + *(const f32x4*)(lnb + c0 + 4);
;                 const f32x4 a0 = __builtin_elementwise_abs(v[h][j][0]), a1 = __builtin_elementwise_abs(v[h][j][1]); am = fmaxf(am, fmaxf(fmaxf(fmaxf(a0.x, a0.y), fmaxf(a0.z, a0.w)), fmaxf(fmaxf(a1.x, a1.y), fmaxf(a1.z, a1.w)))); }
;             if (last) {
; #pragma unroll
;                 for (int j = 0; j < 2; ++j) { const int c0 = lane * 8 + 512 * j; *(f32x4*)(OUT + (size_t)tok * DM + c0) = v[h][j][0]; *(f32x4*)(OUT + (size_t)tok * DM + c0 + 4) = v[h][j][1]; } }
;             else {
;                 am = fmaxf(wave_max(am, lane), 1e-20f); const float inv = 127.f / am; if (lane == 0) SX[tok] = am * (1.f / 127.f);
; #pragma unroll
;                 for (int j = 0; j < 2; ++j) { const int c0 = lane * 8 + 512 * j; const f32x4 x0 = v[h][j][0], x1 = v[h][j][1];
;                     u32x4 w; w.x = pk2(x0.x, x0.y); w.y = pk2(x0.z, x0.w); w.z = pk2(x1.x, x1.y); w.w = pk2(x1.z, x1.w); *(u32x4*)(XB + (size_t)tok * DM + c0) = w;
;                     if (FP6_IN) { const unsigned pk[4] = {pk2(x0.x * QS_XQ, x0.y * QS_XQ), pk2(x0.z * QS_XQ, x0.w * QS_XQ), pk2(x1.x * QS_XQ, x1.y * QS_XQ), pk2(x1.z * QS_XQ, x1.w * QS_XQ)};
;                         store_fp6_quad(XQ + (size_t)tok * DM, (lane >> 2) + 16 * j, pk, lane, j); }
.LBB0_942:
	v_cvt_pk_bf16_f32 v0, v60, v61
	s_waitcnt lgkmcnt(0)
	v_cvt_pk_bf16_f32 v1, v62, v63
	v_lshl_add_u64 v[78:79], v[114:115], 0, s[22:23]
	v_cvt_pk_bf16_f32 v2, v64, v65
	v_cvt_pk_bf16_f32 v3, v66, v67
	global_store_dwordx4 v[78:79], v[0:3], off
	s_lshl_b64 s[14:15], s[20:21], 10
	v_mul_f32_e32 v4, 0x3fe00000, v67
	v_mul_f32_e32 v0, 0x3fe00000, v60
	v_mul_f32_e32 v1, 0x3fe00000, v61
	v_cvt_pk_bf16_f32 v1, v0, v1
	v_mul_f32_e32 v0, 0x3fe00000, v62
	v_mul_f32_e32 v2, 0x3fe00000, v63
	v_cvt_pk_bf16_f32 v2, v0, v2
	v_mul_f32_e32 v0, 0x3fe00000, v64
	v_mul_f32_e32 v3, 0x3fe00000, v65
	v_cvt_pk_bf16_f32 v3, v0, v3
	v_mul_f32_e32 v0, 0x3fe00000, v66
	v_cvt_pk_bf16_f32 v15, v0, v4
	v_lshl_add_u64 v[76:77], v[102:103], 0, s[14:15]
	v_mov_b32_dpp v4, v1 quad_perm:[1,1,1,1] row_mask:0xf bank_mask:0xf bound_ctrl:1
	v_mov_b32_dpp v0, v1 quad_perm:[0,0,0,0] row_mask:0xf bank_mask:0xf bound_ctrl:1
	v_mov_b32_dpp v8, v1 quad_perm:[2,2,2,2] row_mask:0xf bank_mask:0xf bound_ctrl:1
	v_mov_b32_dpp v12, v1 quad_perm:[3,3,3,3] row_mask:0xf bank_mask:0xf bound_ctrl:1
	v_mov_b32_dpp v1, v2 quad_perm:[0,0,0,0] row_mask:0xf bank_mask:0xf bound_ctrl:1
	v_mov_b32_dpp v5, v2 quad_perm:[1,1,1,1] row_mask:0xf bank_mask:0xf bound_ctrl:1
	v_mov_b32_dpp v9, v2 quad_perm:[2,2,2,2] row_mask:0xf bank_mask:0xf bound_ctrl:1
	v_mov_b32_dpp v13, v2 quad_perm:[3,3,3,3] row_mask:0xf bank_mask:0xf bound_ctrl:1
	v_mov_b32_dpp v2, v3 quad_perm:[0,0,0,0] row_mask:0xf bank_mask:0xf bound_ctrl:1
	v_mov_b32_dpp v6, v3 quad_perm:[1,1,1,1] row_mask:0xf bank_mask:0xf bound_ctrl:1
	v_mov_b32_dpp v10, v3 quad_perm:[2,2,2,2] row_mask:0xf bank_mask:0xf bound_ctrl:1
	v_mov_b32_dpp v14, v3 quad_perm:[3,3,3,3] row_mask:0xf bank_mask:0xf bound_ctrl:1
	v_mov_b32_dpp v3, v15 quad_perm:[0,0,0,0] row_mask:0xf bank_mask:0xf bound_ctrl:1
	v_mov_b32_dpp v7, v15 quad_perm:[1,1,1,1] row_mask:0xf bank_mask:0xf bound_ctrl:1
	v_mov_b32_dpp v11, v15 quad_perm:[2,2,2,2] row_mask:0xf bank_mask:0xf bound_ctrl:1
	v_mov_b32_dpp v15, v15 quad_perm:[3,3,3,3] row_mask:0xf bank_mask:0xf bound_ctrl:1
	s_and_saveexec_b64 s[14:15], s[8:9]
	s_cbranch_execz .LBB0_944
	v_lshl_add_u64 v[86:87], v[76:77], 0, v[100:101]
	v_cvt_scalef32_pk32_fp6_bf16 v[80:85], v[0:15], 1.0
	v_mov_b32_e32 v0, v84
	v_mov_b32_e32 v1, v85
	v_mov_b32_e32 v2, v84
	v_mov_b32_e32 v3, v85
	global_store_dwordx4 v[86:87], v[80:83], off
	global_store_dwordx4 v[86:87], v[0:3], off offset:64

; __device__ __forceinline__ unsigned pk2(float lo, float hi) { unsigned r; asm("v_cvt_pk_bf16_f32 %0, %1, %2" : "=v"(r) : "v"(lo), "v"(hi)); return r; }
; __device__ __forceinline__ void phase_combine(CArgs a, LAS unsigned char* lds, int L, int wv, int xw  ) {
;     ...
;             float am = 0.f;
; #pragma unroll
;             for (int j = 0; j < 2; ++j) { const int c0 = lane * 8 + 512 * j;
;                 v[h][j][0] = v[h][j][0] * rstd * *(const f32x4*)(lng + c0) + *(const f32x4*)(lnb + c0); v[h][j][1] = v[h][j][1] * rstd * *(const f32x4*)(lng + c0 + 4) + *(const f32x4*)(lnb + c0 + 4);
;                 const f32x4 a0 = __builtin_elementwise_abs(v[h][j][0]), a1 = __builtin_elementwise_abs(v[h][j][1]); am = fmaxf(am, fmaxf(fmaxf(fmaxf(a0.x, a0.y), fmaxf(a0.z, a0.w)), fmaxf(fmaxf(a1.x, a1.y), fmaxf(a1.z, a1.w)))); }
;             if (last) {
; #pragma unroll
;                 for (int j = 0; j < 2; ++j) { const int c0 = lane * 8 + 512 * j; *(f32x4*)(OUT + (size_t)tok * DM + c0) = v[h][j][0]; *(f32x4*)(OUT + (size_t)tok * DM + c0 + 4) = v[h][j][1]; } }
;             else {
;                 am = fmaxf(wave_max(am, lane), 1e-20f); const float inv = 127.f / am; if (lane == 0) SX[tok] = am * (1.f / 127.f);
; #pragma unroll
;                 for (int j = 0; j < 2; ++j) { const int c0 = lane * 8 + 512 * j; const f32x4 x0 = v[h][j][0], x1 = v[h][j][1];
;                     u32x4 w; w.x = pk2(x0.x, x0.y); w.y = pk2(x0.z, x0.w); w.z = pk2(x1.x, x1.y); w.w = pk2(x1.z, x1.w); *(u32x4*)(XB + (size_t)tok * DM + c0) = w;
;                     if (FP6_IN) { const unsigned pk[4] = {pk2(x0.x * QS_XQ, x0.y * QS_XQ), pk2(x0.z * QS_XQ, x0.w * QS_XQ), pk2(x1.x * QS_XQ, x1.y * QS_XQ), pk2(x1.z * QS_XQ, x1.w * QS_XQ)};
;                         store_fp6_quad(XQ + (size_t)tok * DM, (lane >> 2) + 16 * j, pk, lane, j); }
.LBB0_952:
	v_cvt_pk_bf16_f32 v0, v16, v17
	s_waitcnt lgkmcnt(0)
	v_cvt_pk_bf16_f32 v1, v18, v19
	v_lshl_add_u64 v[34:35], v[114:115], 0, s[18:19]
	v_cvt_pk_bf16_f32 v2, v20, v21
	v_cvt_pk_bf16_f32 v3, v22, v23
	global_store_dwordx4 v[34:35], v[0:3], off
	s_lshl_b64 s[12:13], s[16:17], 10
	v_mul_f32_e32 v4, 0x3fe00000, v23
	v_mul_f32_e32 v0, 0x3fe00000, v16
	v_mul_f32_e32 v1, 0x3fe00000, v17
	v_cvt_pk_bf16_f32 v1, v0, v1
	v_mul_f32_e32 v0, 0x3fe00000, v18
	v_mul_f32_e32 v2, 0x3fe00000, v19
	v_cvt_pk_bf16_f32 v2, v0, v2
	v_mul_f32_e32 v0, 0x3fe00000, v20
	v_mul_f32_e32 v3, 0x3fe00000, v21
	v_cvt_pk_bf16_f32 v3, v0, v3
	v_mul_f32_e32 v0, 0x3fe00000, v22
	v_cvt_pk_bf16_f32 v15, v0, v4
	v_lshl_add_u64 v[32:33], v[102:103], 0, s[12:13]
	v_mov_b32_dpp v4, v1 quad_perm:[1,1,1,1] row_mask:0xf bank_mask:0xf bound_ctrl:1
	v_mov_b32_dpp v0, v1 quad_perm:[0,0,0,0] row_mask:0xf bank_mask:0xf bound_ctrl:1
	v_mov_b32_dpp v8, v1 quad_perm:[2,2,2,2] row_mask:0xf bank_mask:0xf bound_ctrl:1
	v_mov_b32_dpp v12, v1 quad_perm:[3,3,3,3] row_mask:0xf bank_mask:0xf bound_ctrl:1
	v_mov_b32_dpp v1, v2 quad_perm:[0,0,0,0] row_mask:0xf bank_mask:0xf bound_ctrl:1
	v_mov_b32_dpp v5, v2 quad_perm:[1,1,1,1] row_mask:0xf bank_mask:0xf bound_ctrl:1
	v_mov_b32_dpp v9, v2 quad_perm:[2,2,2,2] row_mask:0xf bank_mask:0xf bound_ctrl:1
	v_mov_b32_dpp v13, v2 quad_perm:[3,3,3,3] row_mask:0xf bank_mask:0xf bound_ctrl:1
	v_mov_b32_dpp v2, v3 quad_perm:[0,0,0,0] row_mask:0xf bank_mask:0xf bound_ctrl:1
	v_mov_b32_dpp v6, v3 quad_perm:[1,1,1,1] row_mask:0xf bank_mask:0xf bound_ctrl:1
	v_mov_b32_dpp v10, v3 quad_perm:[2,2,2,2] row_mask:0xf bank_mask:0xf bound_ctrl:1
	v_mov_b32_dpp v14, v3 quad_perm:[3,3,3,3] row_mask:0xf bank_mask:0xf bound_ctrl:1
	v_mov_b32_dpp v3, v15 quad_perm:[0,0,0,0] row_mask:0xf bank_mask:0xf bound_ctrl:1
	v_mov_b32_dpp v7, v15 quad_perm:[1,1,1,1] row_mask:0xf bank_mask:0xf bound_ctrl:1
	v_mov_b32_dpp v11, v15 quad_perm:[2,2,2,2] row_mask:0xf bank_mask:0xf bound_ctrl:1
	v_mov_b32_dpp v15, v15 quad_perm:[3,3,3,3] row_mask:0xf bank_mask:0xf bound_ctrl:1
	s_and_saveexec_b64 s[12:13], s[8:9]
	s_cbranch_execz .LBB0_954
	v_lshl_add_u64 v[42:43], v[32:33], 0, v[100:101]
	v_cvt_scalef32_pk32_fp6_bf16 v[36:41], v[0:15], 1.0
	v_mov_b32_e32 v0, v40
	v_mov_b32_e32 v1, v41
	v_mov_b32_e32 v2, v40
	v_mov_b32_e32 v3, v41
	global_store_dwordx4 v[42:43], v[36:39], off
	global_store_dwordx4 v[42:43], v[0:3], off offset:64
